# attention: resident Q-rope fragments + ds_reads first after the barrier, DMA groups behind the first five QK^T MFMAs, rope address VALU after the reads
# baseline (speedup 1.0000x reference)
.LBB0_757:
	ds_read_b128 v[64:67], v180 offset:49152
	ds_read_b128 v[68:71], v180 offset:57344
	ds_read_b128 v[200:203], v181 offset:49152
	ds_read_b128 v[226:229], v181 offset:57344
	ds_read_b128 v[230:233], v182 offset:49152
	ds_read_b128 v[234:237], v182 offset:57344
	ds_read_b128 v[238:241], v183 offset:49152
	ds_read_b128 v[242:245], v183 offset:57344
	s_add_i32 s6, 0, 0x12000
	v_add_u32_e32 v199, s6, v170
	v_add_u32_e32 v204, s6, v171
	v_add_u32_e32 v205, s6, v172
	s_waitcnt lgkmcnt(7)
	v_mfma_f32_32x32x16_bf16 v[80:95], v[64:67], v[124:127], 0
	s_add_i32 s12, s64, -1
	s_sub_i32 s80, s11, 64
	s_cmp_lt_u32 s12, 3
	s_cselect_b32 s80, s10, s80
	s_mul_i32 s81, s80, 0xc00
	s_add_i32 s85, s82, 0x8000
	s_mov_b32 m0, s85
	s_add_i32 s85, s82, 0x10000
	buffer_load_dwordx4 v154, s[72:75], s81 offen lds
	v_exp_f32_e32 v216, v128
	v_add_f32_e32 v128, 0, v222
	v_add_f32_e32 v128, v224, v128
	v_add_f32_e32 v128, v220, v128
	v_add_f32_e32 v128, v223, v128
	v_add_f32_e32 v128, v219, v128
	v_add_f32_e32 v128, v221, v128
	s_waitcnt lgkmcnt(6)
	v_mfma_f32_32x32x16_bf16 v[64:79], v[68:71], v[124:127], 0
	s_mov_b32 m0, s85
	s_add_i32 s85, s82, 0xa000
	buffer_load_dwordx4 v155, s[72:75], s81 offen lds
	v_add_f32_e32 v128, v217, v128
	v_add_f32_e32 v128, v218, v128
	v_add_f32_e32 v128, v212, v128
	v_add_f32_e32 v128, v214, v128
	v_add_f32_e32 v128, v211, v128
	v_add_f32_e32 v128, v213, v128
	v_exp_f32_e32 v138, v138
	s_waitcnt lgkmcnt(5)
	v_mfma_f32_32x32x16_bf16 v[80:95], v[200:203], v[120:123], v[80:95]
	s_mov_b32 m0, s85
	s_add_i32 s81, s81, 0x18000
	buffer_load_dwordx4 v154, s[72:75], s81 offen lds
	v_add_f32_e32 v128, v208, v128
	v_exp_f32_e32 v139, v139
	v_add_f32_e32 v128, v210, v128
	v_exp_f32_e32 v164, v136
	v_add_f32_e32 v128, v207, v128
	v_exp_f32_e32 v137, v137
	v_add_f32_e32 v128, v209, v128
	s_waitcnt lgkmcnt(4)
	v_mfma_f32_32x32x16_bf16 v[64:79], v[226:229], v[120:123], v[64:79]
	s_lshl_b32 s81, s83, 11
	s_add_i32 s85, s82, 0x4000
	s_mov_b32 m0, s85
	s_add_i32 s85, s82, 0x6000
	buffer_load_dwordx4 v196, s[76:79], s81 offen lds
	ds_read_b128 v[200:203], v184 offset:49152
	ds_read_b128 v[226:229], v184 offset:57344
	v_exp_f32_e32 v165, v132
	v_add_f32_e32 v128, v138, v128
	v_add_f32_e32 v128, v139, v128
	v_exp_f32_e32 v206, v130
	v_add_f32_e32 v128, v164, v128
	v_exp_f32_e32 v215, v131
	s_waitcnt lgkmcnt(5)
	v_mfma_f32_32x32x16_bf16 v[80:95], v[230:233], v[116:119], v[80:95]
	s_mov_b32 m0, s85
	s_add_i32 s81, s81, 0x10000
	buffer_load_dwordx4 v196, s[76:79], s81 offen lds
	s_mov_b32 s84, s80
	v_add_f32_e32 v128, v137, v128
	v_add_f32_e32 v128, v165, v128
	v_exp_f32_e32 v225, v129
	v_exp_f32_e32 v162, v162
	v_exp_f32_e32 v163, v163
	v_exp_f32_e32 v160, v160
	v_exp_f32_e32 v161, v161
	s_waitcnt lgkmcnt(4)
	v_mfma_f32_32x32x16_bf16 v[64:79], v[234:237], v[116:119], v[64:79]
	ds_read_b128 v[230:233], v185 offset:49152
	ds_read_b128 v[234:237], v185 offset:57344
	v_cvt_pk_bf16_f32 v129, v220, v223
	v_cvt_pk_bf16_f32 v130, v219, v221
	v_cvt_pk_bf16_f32 v131, v217, v218
	v_cvt_pk_bf16_f32 v132, v212, v214
	v_cvt_pk_bf16_f32 v136, v138, v139
	v_cvt_pk_bf16_f32 v137, v164, v137
	s_waitcnt lgkmcnt(5)
	v_mfma_f32_32x32x16_bf16 v[80:95], v[238:241], v[112:115], v[80:95]
	v_cvt_pk_bf16_f32 v139, v206, v215
	v_permlane32_swap_b32_e32 v129, v131
	s_nop 0
	v_permlane32_swap_b32_e32 v137, v139
	s_waitcnt lgkmcnt(4)
	v_mfma_f32_32x32x16_bf16 v[64:79], v[242:245], v[112:115], v[64:79]
	ds_read_b128 v[238:241], v186 offset:49152
	ds_read_b128 v[242:245], v186 offset:57344
	s_waitcnt lgkmcnt(5)
	v_mfma_f32_32x32x16_bf16 v[80:95], v[200:203], v[108:111], v[80:95]
	s_waitcnt lgkmcnt(4)
	v_mfma_f32_32x32x16_bf16 v[64:79], v[226:229], v[108:111], v[64:79]
	ds_read_b128 v[200:203], v187 offset:49152
	ds_read_b128 v[226:229], v187 offset:57344
	s_waitcnt lgkmcnt(5)
	v_mfma_f32_32x32x16_bf16 v[80:95], v[230:233], v[104:107], v[80:95]
	s_waitcnt lgkmcnt(4)
	v_mfma_f32_32x32x16_bf16 v[64:79], v[234:237], v[104:107], v[64:79]
	ds_read_b128 v[230:233], v199
	ds_read_b128 v[234:237], v199 offset:4096
	s_waitcnt lgkmcnt(5)
	v_mfma_f32_32x32x16_bf16 v[80:95], v[238:241], v[100:103], v[80:95]
	s_waitcnt lgkmcnt(4)
	v_mfma_f32_32x32x16_bf16 v[64:79], v[242:245], v[100:103], v[64:79]
	ds_read_b128 v[238:241], v204
	ds_read_b128 v[242:245], v204 offset:4096
	v_add_u32_e32 v204, s6, v173
	s_waitcnt lgkmcnt(5)
	v_mfma_f32_32x32x16_bf16 v[80:95], v[200:203], v[96:99], v[80:95]
	s_waitcnt lgkmcnt(4)
	v_mfma_f32_32x32x16_bf16 v[64:79], v[226:229], v[96:99], v[64:79]
	ds_read_b128 v[200:203], v205
	ds_read_b128 v[226:229], v205 offset:4096
	s_waitcnt lgkmcnt(5)
	v_mfma_f32_32x32x16_bf16 v[80:95], v[230:233], v[142:145], v[80:95]
	s_waitcnt lgkmcnt(4)
	v_mfma_f32_32x32x16_bf16 v[64:79], v[234:237], v[142:145], v[64:79]
	ds_read_b128 v[230:233], v204
	ds_read_b128 v[234:237], v204 offset:4096
	s_waitcnt lgkmcnt(5)
	v_mfma_f32_32x32x16_bf16 v[80:95], v[238:241], v[146:149], v[80:95]
	s_waitcnt lgkmcnt(4)
	v_mfma_f32_32x32x16_bf16 v[64:79], v[242:245], v[146:149], v[64:79]
	s_waitcnt lgkmcnt(3)
	v_mfma_f32_32x32x16_bf16 v[80:95], v[200:203], v[150:153], v[80:95]
	v_exp_f32_e32 v205, v133
	v_cvt_pk_bf16_f32 v133, v211, v213
	v_cvt_pk_bf16_f32 v138, v165, v205
	v_add_f32_e32 v128, v205, v128
	v_add_f32_e32 v128, v206, v128
	v_add_f32_e32 v128, v215, v128
	s_waitcnt lgkmcnt(2)
	v_mfma_f32_32x32x16_bf16 v[64:79], v[226:229], v[150:153], v[64:79]
	v_add_f32_e32 v128, v216, v128
	v_add_f32_e32 v128, v225, v128
	v_add_f32_e32 v128, v162, v128
	v_add_f32_e32 v128, v163, v128
	v_add_f32_e32 v128, v160, v128
	v_add_f32_e32 v128, v161, v128
	s_waitcnt lgkmcnt(1)
	v_mfma_f32_32x32x16_bf16 v[80:95], v[230:233], v[156:159], v[80:95]
	v_exp_f32_e32 v226, v134
	v_exp_f32_e32 v227, v135
	v_cvt_pk_bf16_f32 v134, v208, v210
	v_cvt_pk_bf16_f32 v135, v207, v209
	v_add_f32_e32 v128, v226, v128
	v_add_f32_e32 v203, v227, v128
	v_mov_b32_e32 v204, v203
	s_waitcnt lgkmcnt(0)
	v_mfma_f32_32x32x16_bf16 v[64:79], v[234:237], v[156:159], v[64:79]
	s_nop 0
	v_permlane32_swap_b32_e32 v203, v204
	v_cvt_pk_bf16_f32 v128, v222, v224
	v_cvt_pk_bf16_f32 v208, v216, v225
	v_cvt_pk_bf16_f32 v209, v162, v163
	v_cvt_pk_bf16_f32 v210, v160, v161
	v_cvt_pk_bf16_f32 v211, v226, v227
	v_permlane32_swap_b32_e32 v132, v134
	v_permlane32_swap_b32_e32 v128, v130
	v_permlane32_swap_b32_e32 v133, v135
	v_permlane32_swap_b32_e32 v136, v138
	v_permlane32_swap_b32_e32 v208, v210
	v_permlane32_swap_b32_e32 v209, v211
	ds_read_b64_tr_b16 v[160:161], v167 offset:0
	ds_read_b64_tr_b16 v[162:163], v167 offset:0x800
	ds_read_b64_tr_b16 v[232:233], v167 offset:0x1000
	ds_read_b64_tr_b16 v[234:235], v167 offset:0x1800
	ds_read_b64_tr_b16 v[236:237], v167 offset:0x2000
	ds_read_b64_tr_b16 v[238:239], v167 offset:0x2800
	ds_read_b64_tr_b16 v[240:241], v167 offset:0x3000
	ds_read_b64_tr_b16 v[242:243], v167 offset:0x3800
	v_max_f32_e32 v164, v81, v81
	v_max_f32_e32 v165, v80, v80
	v_max_f32_e32 v164, v165, v164
	v_max3_f32 v164, v164, v82, v83
	v_max3_f32 v164, v164, v84, v85
	v_max3_f32 v164, v164, v86, v87
	v_max3_f32 v164, v164, v88, v89
	v_max3_f32 v164, v164, v90, v91
	v_max3_f32 v164, v164, v92, v93
	v_max3_f32 v164, v164, v94, v95
	s_waitcnt lgkmcnt(0)
	v_mfma_f32_32x32x16_bf16 v[16:31], v[128:131], v[160:163], v[16:31]
	v_max3_f32 v160, v164, v64, v65
	v_max3_f32 v160, v160, v66, v67
	v_max3_f32 v160, v160, v68, v69
	v_mfma_f32_32x32x16_bf16 v[16:31], v[132:135], v[232:235], v[16:31]
	ds_read_b64_tr_b16 v[232:233], v167 offset:0x200
	ds_read_b64_tr_b16 v[234:235], v167 offset:0xa00
	v_max3_f32 v160, v160, v70, v71
	v_max3_f32 v160, v160, v72, v73
	v_max3_f32 v160, v160, v74, v75
	v_mfma_f32_32x32x16_bf16 v[16:31], v[136:139], v[236:239], v[16:31]
	ds_read_b64_tr_b16 v[236:237], v167 offset:0x1200
	ds_read_b64_tr_b16 v[238:239], v167 offset:0x1a00
	ds_read_b64_tr_b16 v[244:245], v167 offset:0x2200
	ds_read_b64_tr_b16 v[246:247], v167 offset:0x2a00
	ds_read_b64_tr_b16 v[248:249], v167 offset:0x3200
	ds_read_b64_tr_b16 v[250:251], v167 offset:0x3a00
	v_max3_f32 v160, v160, v76, v77
	v_max3_f32 v160, v160, v78, v79
	v_mov_b32_e32 v161, v160
	v_mfma_f32_32x32x16_bf16 v[16:31], v[208:211], v[240:243], v[16:31]
	v_max_f32_e32 v162, v198, v198
	v_permlane32_swap_b32_e32 v160, v161
	v_max_f32_e32 v161, v161, v161
	v_max_f32_e32 v160, v160, v160
	v_max_f32_e32 v160, v160, v161
	s_waitcnt lgkmcnt(0)
	v_mfma_f32_32x32x16_bf16 v[32:47], v[128:131], v[232:235], v[32:47]
	ds_read_b64_tr_b16 v[232:233], v167 offset:0x400
	ds_read_b64_tr_b16 v[234:235], v167 offset:0xc00
	v_sub_f32_e32 v161, v160, v198
	v_max_f32_e32 v160, v162, v160
	v_sub_f32_e32 v162, v198, v160
	v_mul_f32_e32 v162, 0x3dd53b94, v162
	v_exp_f32_e32 v162, v162
	v_mfma_f32_32x32x16_bf16 v[32:47], v[132:135], v[236:239], v[32:47]
	ds_read_b64_tr_b16 v[236:237], v167 offset:0x1400
	ds_read_b64_tr_b16 v[238:239], v167 offset:0x1c00
	ds_read_b64_tr_b16 v[240:241], v167 offset:0x2400
	ds_read_b64_tr_b16 v[242:243], v167 offset:0x2c00
	v_cmp_ge_f32_e32 vcc, s48, v161
	s_cmp_eq_u64 vcc, exec
	s_cselect_b64 s[6:7], -1, 0
	v_cndmask_b32_e64 v206, v162, 1.0, s[6:7]
	v_cndmask_b32_e64 v160, v160, v198, s[6:7]
	v_mul_f32_e32 v205, 0xbdd53b94, v160
	v_cmp_gt_f32_e32 vcc, 1.0, v206
	v_mfma_f32_32x32x16_bf16 v[32:47], v[136:139], v[244:247], v[32:47]
	ds_read_b64_tr_b16 v[244:245], v167 offset:0x3400
	ds_read_b64_tr_b16 v[246:247], v167 offset:0x3c00
	v_fmamk_f32 v87, v87, 0x3dd53b94, v205
	v_fmamk_f32 v80, v80, 0x3dd53b94, v205
	v_fmamk_f32 v81, v81, 0x3dd53b94, v205
	v_fmamk_f32 v82, v82, 0x3dd53b94, v205
	v_fmamk_f32 v83, v83, 0x3dd53b94, v205
	v_mfma_f32_32x32x16_bf16 v[32:47], v[208:211], v[248:251], v[32:47]
	v_fmamk_f32 v84, v84, 0x3dd53b94, v205
	v_fmamk_f32 v85, v85, 0x3dd53b94, v205
	v_fmamk_f32 v86, v86, 0x3dd53b94, v205
	v_fmamk_f32 v88, v88, 0x3dd53b94, v205
	v_fmamk_f32 v89, v89, 0x3dd53b94, v205
	s_waitcnt lgkmcnt(0)
	v_mfma_f32_32x32x16_bf16 v[0:15], v[128:131], v[232:235], v[0:15]
	ds_read_b64_tr_b16 v[232:233], v167 offset:0x600
	ds_read_b64_tr_b16 v[234:235], v167 offset:0xe00
	v_fmamk_f32 v90, v90, 0x3dd53b94, v205
	v_fmamk_f32 v91, v91, 0x3dd53b94, v205
	v_fmamk_f32 v92, v92, 0x3dd53b94, v205
	v_fmamk_f32 v93, v93, 0x3dd53b94, v205
	v_fmamk_f32 v94, v94, 0x3dd53b94, v205
	v_mfma_f32_32x32x16_bf16 v[0:15], v[132:135], v[236:239], v[0:15]
	ds_read_b64_tr_b16 v[236:237], v167 offset:0x1600
	ds_read_b64_tr_b16 v[238:239], v167 offset:0x1e00
	v_fmamk_f32 v95, v95, 0x3dd53b94, v205
	v_fmamk_f32 v215, v64, 0x3dd53b94, v205
	v_fmamk_f32 v216, v65, 0x3dd53b94, v205
	v_fmamk_f32 v217, v66, 0x3dd53b94, v205
	v_fmamk_f32 v218, v67, 0x3dd53b94, v205
	v_mfma_f32_32x32x16_bf16 v[0:15], v[136:139], v[240:243], v[0:15]
	ds_read_b64_tr_b16 v[240:241], v167 offset:0x2600
	ds_read_b64_tr_b16 v[242:243], v167 offset:0x2e00
	ds_read_b64_tr_b16 v[248:249], v167 offset:0x3600
	ds_read_b64_tr_b16 v[250:251], v167 offset:0x3e00
	v_fmamk_f32 v219, v68, 0x3dd53b94, v205
	v_fmamk_f32 v212, v73, 0x3dd53b94, v205
	v_fmamk_f32 v213, v74, 0x3dd53b94, v205
	v_fmamk_f32 v214, v75, 0x3dd53b94, v205
	v_mfma_f32_32x32x16_bf16 v[0:15], v[208:211], v[244:247], v[0:15]
	v_fmamk_f32 v207, v76, 0x3dd53b94, v205
	v_fmamk_f32 v220, v77, 0x3dd53b94, v205
	v_fmamk_f32 v221, v78, 0x3dd53b94, v205
	s_waitcnt lgkmcnt(0)
	v_mfma_f32_32x32x16_bf16 v[48:63], v[128:131], v[232:235], v[48:63]
	v_exp_f32_e32 v128, v80
	v_exp_f32_e32 v129, v82
	v_exp_f32_e32 v130, v84
	v_exp_f32_e32 v131, v86
	v_mfma_f32_32x32x16_bf16 v[48:63], v[132:135], v[236:239], v[48:63]
	v_exp_f32_e32 v132, v88
	v_exp_f32_e32 v133, v90
	v_exp_f32_e32 v134, v92
	v_exp_f32_e32 v135, v94
	v_mfma_f32_32x32x16_bf16 v[48:63], v[136:139], v[240:243], v[48:63]
	v_exp_f32_e32 v139, v89
	v_exp_f32_e32 v138, v91
	v_exp_f32_e32 v137, v93
	v_exp_f32_e32 v136, v95
	v_mfma_f32_32x32x16_bf16 v[48:63], v[208:211], v[248:251], v[48:63]
	v_exp_f32_e32 v161, v87
	v_exp_f32_e32 v198, v81
	v_exp_f32_e32 v163, v83
	v_exp_f32_e32 v162, v85
	v_fmamk_f32 v208, v69, 0x3dd53b94, v205
	v_fmamk_f32 v209, v70, 0x3dd53b94, v205
	v_fmamk_f32 v210, v71, 0x3dd53b94, v205
	v_fmamk_f32 v211, v72, 0x3dd53b94, v205
	v_fmac_f32_e32 v205, 0x3dd53b94, v79
	s_cbranch_vccz .LBB0_761
	s_and_saveexec_b64 s[8:9], s[4:5]
	ds_write_b32 v189, v206 offset:128
	s_or_b64 exec, exec, s[8:9]
	s_waitcnt lgkmcnt(0)
	v_add_u32_e32 v248, s62, v169
	ds_read_b128 v[232:235], v248 offset:224
	ds_read_b128 v[236:239], v248 offset:192
	ds_read_b128 v[240:243], v248 offset:160
	ds_read_b128 v[244:247], v248 offset:128
	s_waitcnt lgkmcnt(3)
	v_pk_mul_f32 v[28:29], v[28:29], v[232:233]
	s_waitcnt lgkmcnt(2)
	v_pk_mul_f32 v[24:25], v[24:25], v[236:237]
	s_waitcnt lgkmcnt(1)
	v_pk_mul_f32 v[20:21], v[20:21], v[240:241]
	v_pk_mul_f32 v[30:31], v[30:31], v[234:235]
	v_pk_mul_f32 v[26:27], v[26:27], v[238:239]
	v_pk_mul_f32 v[22:23], v[22:23], v[242:243]
	s_waitcnt lgkmcnt(0)
	v_pk_mul_f32 v[18:19], v[18:19], v[246:247]
	v_pk_mul_f32 v[16:17], v[16:17], v[244:245]
	v_pk_mul_f32 v[44:45], v[44:45], v[232:233]
	v_pk_mul_f32 v[40:41], v[40:41], v[236:237]
	v_pk_mul_f32 v[36:37], v[36:37], v[240:241]
	v_pk_mul_f32 v[46:47], v[46:47], v[234:235]
	v_pk_mul_f32 v[42:43], v[42:43], v[238:239]
	v_pk_mul_f32 v[38:39], v[38:39], v[242:243]
	v_pk_mul_f32 v[34:35], v[34:35], v[246:247]
	v_pk_mul_f32 v[32:33], v[32:33], v[244:245]
	v_pk_mul_f32 v[12:13], v[12:13], v[232:233]
	v_pk_mul_f32 v[8:9], v[8:9], v[236:237]
	v_pk_mul_f32 v[4:5], v[4:5], v[240:241]
	v_pk_mul_f32 v[14:15], v[14:15], v[234:235]
	v_pk_mul_f32 v[10:11], v[10:11], v[238:239]
	v_pk_mul_f32 v[6:7], v[6:7], v[242:243]
	v_pk_mul_f32 v[2:3], v[2:3], v[246:247]
	v_pk_mul_f32 v[0:1], v[0:1], v[244:245]
	v_pk_mul_f32 v[60:61], v[60:61], v[232:233]
	v_pk_mul_f32 v[56:57], v[56:57], v[236:237]
	v_pk_mul_f32 v[52:53], v[52:53], v[240:241]
	v_pk_mul_f32 v[62:63], v[62:63], v[234:235]
	v_pk_mul_f32 v[58:59], v[58:59], v[238:239]
	v_pk_mul_f32 v[54:55], v[54:55], v[242:243]
	v_pk_mul_f32 v[50:51], v[50:51], v[246:247]
	v_pk_mul_f32 v[48:49], v[48:49], v[244:245]
.LBB0_761:
	s_waitcnt vmcnt(0) lgkmcnt(0)
	s_barrier
	ds_read_b128 v[64:67], v180 offset:32768
	ds_read_b128 v[68:71], v180 offset:40960
	ds_read_b128 v[222:225], v181 offset:32768
	ds_read_b128 v[226:229], v181 offset:40960
	ds_read_b128 v[230:233], v182 offset:32768
	ds_read_b128 v[234:237], v182 offset:40960
	ds_read_b128 v[238:241], v183 offset:32768
	ds_read_b128 v[242:245], v183 offset:40960
	v_exp_f32_e32 v164, v215
	v_add_f32_e32 v215, 0, v128
	s_waitcnt lgkmcnt(7)
	v_mfma_f32_32x32x16_bf16 v[80:95], v[64:67], v[124:127], 0
	s_add_i32 s80, s10, 64
	s_cmp_lt_u32 s12, 2
	s_cselect_b32 s80, s80, s11
	s_mul_i32 s81, s80, 0xc00
	s_add_i32 s85, s82, 0xc000
	s_mov_b32 m0, s85
	s_add_i32 s85, s82, 0x12000
	buffer_load_dwordx4 v154, s[72:75], s81 offen lds
	v_add_f32_e32 v215, v198, v215
	v_add_f32_e32 v215, v129, v215
	v_add_f32_e32 v215, v163, v215
	v_add_f32_e32 v215, v130, v215
	v_add_f32_e32 v215, v162, v215
	v_add_f32_e32 v215, v131, v215
	v_add_f32_e32 v215, v161, v215
	s_waitcnt lgkmcnt(6)
	v_mfma_f32_32x32x16_bf16 v[64:79], v[68:71], v[124:127], 0
	s_mov_b32 m0, s85
	s_add_i32 s85, s82, 0xe000
	buffer_load_dwordx4 v155, s[72:75], s81 offen lds
	v_add_f32_e32 v215, v132, v215
	v_add_f32_e32 v215, v139, v215
	v_add_f32_e32 v215, v133, v215
	v_add_f32_e32 v215, v138, v215
	v_add_f32_e32 v215, v134, v215
	v_exp_f32_e32 v165, v216
	v_add_f32_e32 v215, v137, v215
	s_waitcnt lgkmcnt(5)
	v_mfma_f32_32x32x16_bf16 v[80:95], v[222:225], v[120:123], v[80:95]
	s_mov_b32 m0, s85
	s_add_i32 s81, s81, 0x18000
	buffer_load_dwordx4 v154, s[72:75], s81 offen lds
	v_exp_f32_e32 v217, v217
	v_add_f32_e32 v215, v135, v215
	v_exp_f32_e32 v218, v218
	v_add_f32_e32 v215, v136, v215
	v_exp_f32_e32 v219, v219
	v_add_f32_e32 v215, v164, v215
	v_exp_f32_e32 v208, v208
	s_waitcnt lgkmcnt(4)
	v_mfma_f32_32x32x16_bf16 v[64:79], v[226:229], v[120:123], v[64:79]
	s_lshl_b32 s81, s84, 11
	s_add_i32 s85, s82, 0x0
	s_mov_b32 m0, s85
	s_add_i32 s85, s82, 0x2000
	buffer_load_dwordx4 v196, s[76:79], s81 offen lds
	ds_read_b128 v[222:225], v184 offset:32768
	ds_read_b128 v[226:229], v184 offset:40960
	v_add_f32_e32 v215, v165, v215
	v_exp_f32_e32 v209, v209
	v_add_f32_e32 v215, v217, v215
	v_exp_f32_e32 v210, v210
	v_add_f32_e32 v215, v218, v215
	v_exp_f32_e32 v211, v211
	s_waitcnt lgkmcnt(5)
	v_mfma_f32_32x32x16_bf16 v[80:95], v[230:233], v[116:119], v[80:95]
	s_mov_b32 m0, s85
	s_add_i32 s81, s81, 0x10000
	buffer_load_dwordx4 v196, s[76:79], s81 offen lds
	s_mov_b32 s83, s80
	v_add_f32_e32 v215, v219, v215
	v_exp_f32_e32 v212, v212
	v_add_f32_e32 v215, v208, v215
	v_exp_f32_e32 v213, v213
	v_add_f32_e32 v215, v209, v215
	v_exp_f32_e32 v214, v214
	v_add_f32_e32 v215, v210, v215
	s_waitcnt lgkmcnt(4)
	v_mfma_f32_32x32x16_bf16 v[64:79], v[234:237], v[116:119], v[64:79]
	ds_read_b128 v[230:233], v185 offset:32768
	ds_read_b128 v[234:237], v185 offset:40960
	v_exp_f32_e32 v207, v207
	v_add_f32_e32 v215, v211, v215
	v_exp_f32_e32 v220, v220
	v_add_f32_e32 v215, v212, v215
	v_exp_f32_e32 v221, v221
	v_add_f32_e32 v215, v213, v215
	s_waitcnt lgkmcnt(5)
	v_mfma_f32_32x32x16_bf16 v[80:95], v[238:241], v[112:115], v[80:95]
	v_exp_f32_e32 v205, v205
	v_add_f32_e32 v215, v214, v215
	v_add_f32_e32 v215, v207, v215
	v_add_f32_e32 v215, v220, v215
	v_add_f32_e32 v215, v221, v215
	v_add_f32_e32 v215, v205, v215
	v_mov_b32_e32 v216, v215
	s_waitcnt lgkmcnt(4)
	v_mfma_f32_32x32x16_bf16 v[64:79], v[242:245], v[112:115], v[64:79]
	ds_read_b128 v[238:241], v186 offset:32768
	ds_read_b128 v[242:245], v186 offset:40960
	v_permlane32_swap_b32_e32 v215, v216
	v_cvt_pk_bf16_f32 v128, v128, v198
	v_cvt_pk_bf16_f32 v129, v129, v163
	v_cvt_pk_bf16_f32 v130, v130, v162
	v_cvt_pk_bf16_f32 v131, v131, v161
	s_waitcnt lgkmcnt(5)
	v_mfma_f32_32x32x16_bf16 v[80:95], v[222:225], v[108:111], v[80:95]
	v_cvt_pk_bf16_f32 v132, v132, v139
	v_cvt_pk_bf16_f32 v133, v133, v138
	v_cvt_pk_bf16_f32 v134, v134, v137
	v_cvt_pk_bf16_f32 v135, v135, v136
	v_cvt_pk_bf16_f32 v136, v164, v165
	v_cvt_pk_bf16_f32 v137, v217, v218
	v_cvt_pk_bf16_f32 v138, v219, v208
	s_waitcnt lgkmcnt(4)
	v_mfma_f32_32x32x16_bf16 v[64:79], v[226:229], v[108:111], v[64:79]
	ds_read_b128 v[222:225], v187 offset:32768
	ds_read_b128 v[226:229], v187 offset:40960
	v_cvt_pk_bf16_f32 v139, v209, v210
	v_cvt_pk_bf16_f32 v208, v211, v212
	v_cvt_pk_bf16_f32 v209, v213, v214
	v_cvt_pk_bf16_f32 v210, v207, v220
	v_cvt_pk_bf16_f32 v211, v221, v205
	v_permlane32_swap_b32_e32 v128, v130
	s_waitcnt lgkmcnt(5)
	v_mfma_f32_32x32x16_bf16 v[80:95], v[230:233], v[104:107], v[80:95]
	v_permlane32_swap_b32_e32 v129, v131
	v_permlane32_swap_b32_e32 v132, v134
	v_permlane32_swap_b32_e32 v133, v135
	v_permlane32_swap_b32_e32 v136, v138
	s_waitcnt lgkmcnt(4)
	v_mfma_f32_32x32x16_bf16 v[64:79], v[234:237], v[104:107], v[64:79]
	ds_read_b128 v[230:233], v191
	ds_read_b128 v[234:237], v191 offset:4096
	v_permlane32_swap_b32_e32 v137, v139
	v_permlane32_swap_b32_e32 v208, v210
	v_permlane32_swap_b32_e32 v209, v211
	s_waitcnt lgkmcnt(5)
	v_mfma_f32_32x32x16_bf16 v[80:95], v[238:241], v[100:103], v[80:95]
	s_waitcnt lgkmcnt(4)
	v_mfma_f32_32x32x16_bf16 v[64:79], v[242:245], v[100:103], v[64:79]
	ds_read_b128 v[238:241], v192
	ds_read_b128 v[242:245], v192 offset:4096
	s_waitcnt lgkmcnt(5)
	v_mfma_f32_32x32x16_bf16 v[80:95], v[222:225], v[96:99], v[80:95]
	s_waitcnt lgkmcnt(4)
	v_mfma_f32_32x32x16_bf16 v[64:79], v[226:229], v[96:99], v[64:79]
	ds_read_b128 v[222:225], v193
	ds_read_b128 v[226:229], v193 offset:4096
	s_waitcnt lgkmcnt(5)
	v_mfma_f32_32x32x16_bf16 v[80:95], v[230:233], v[142:145], v[80:95]
	s_waitcnt lgkmcnt(4)
	v_mfma_f32_32x32x16_bf16 v[64:79], v[234:237], v[142:145], v[64:79]
	ds_read_b128 v[230:233], v194
	ds_read_b128 v[234:237], v194 offset:4096
	s_waitcnt lgkmcnt(5)
	v_mfma_f32_32x32x16_bf16 v[80:95], v[238:241], v[146:149], v[80:95]
	s_waitcnt lgkmcnt(4)
	v_mfma_f32_32x32x16_bf16 v[64:79], v[242:245], v[146:149], v[64:79]
	s_waitcnt lgkmcnt(3)
	v_mfma_f32_32x32x16_bf16 v[80:95], v[222:225], v[150:153], v[80:95]
	s_waitcnt lgkmcnt(2)
	v_mfma_f32_32x32x16_bf16 v[64:79], v[226:229], v[150:153], v[64:79]
	s_waitcnt lgkmcnt(1)
	v_mfma_f32_32x32x16_bf16 v[80:95], v[230:233], v[156:159], v[80:95]
	s_waitcnt lgkmcnt(0)
	v_mfma_f32_32x32x16_bf16 v[64:79], v[234:237], v[156:159], v[64:79]
	ds_read_b64_tr_b16 v[238:239], v174 offset:0
	ds_read_b64_tr_b16 v[240:241], v174 offset:0x800
	ds_read_b64_tr_b16 v[242:243], v174 offset:0x1000
	ds_read_b64_tr_b16 v[244:245], v174 offset:0x1800
	ds_read_b64_tr_b16 v[246:247], v174 offset:0x2000
	ds_read_b64_tr_b16 v[248:249], v174 offset:0x2800
	ds_read_b64_tr_b16 v[250:251], v174 offset:0x3000
	ds_read_b64_tr_b16 v[252:253], v174 offset:0x3800
	s_nop 3
	v_max_f32_e32 v161, v81, v81
	v_max_f32_e32 v162, v80, v80
	v_max_f32_e32 v161, v162, v161
	v_max3_f32 v161, v161, v82, v83
	v_max3_f32 v161, v161, v84, v85
	v_max3_f32 v161, v161, v86, v87
	v_max3_f32 v161, v161, v88, v89
	v_max3_f32 v161, v161, v90, v91
	v_max3_f32 v161, v161, v92, v93
	v_max3_f32 v161, v161, v94, v95
	s_waitcnt lgkmcnt(0)
	v_mfma_f32_32x32x16_bf16 v[16:31], v[128:131], v[238:241], v[16:31]
	ds_read_b64_tr_b16 v[238:239], v174 offset:0x200
	ds_read_b64_tr_b16 v[240:241], v174 offset:0xa00
	v_max3_f32 v161, v161, v64, v65
	v_max3_f32 v161, v161, v66, v67
	v_max3_f32 v161, v161, v68, v69
	v_mfma_f32_32x32x16_bf16 v[16:31], v[132:135], v[242:245], v[16:31]
	ds_read_b64_tr_b16 v[242:243], v174 offset:0x1200
	ds_read_b64_tr_b16 v[244:245], v174 offset:0x1a00
	v_max3_f32 v161, v161, v70, v71
	v_max3_f32 v161, v161, v72, v73
	v_max3_f32 v161, v161, v74, v75
	v_mfma_f32_32x32x16_bf16 v[16:31], v[136:139], v[246:249], v[16:31]
	ds_read_b64_tr_b16 v[246:247], v174 offset:0x2200
	ds_read_b64_tr_b16 v[248:249], v174 offset:0x2a00
	ds_read_b64_tr_b16 v[162:163], v174 offset:0x3200
	ds_read_b64_tr_b16 v[164:165], v174 offset:0x3a00
	v_max3_f32 v161, v161, v76, v77
	v_max3_f32 v161, v161, v78, v79
	v_mov_b32_e32 v198, v161
	v_mfma_f32_32x32x16_bf16 v[16:31], v[208:211], v[250:253], v[16:31]
	v_max_f32_e32 v205, v160, v160
	v_permlane32_swap_b32_e32 v161, v198
	v_max_f32_e32 v198, v198, v198
	v_max_f32_e32 v161, v161, v161
	v_max_f32_e32 v161, v161, v198
	s_waitcnt lgkmcnt(0)
	v_mfma_f32_32x32x16_bf16 v[32:47], v[128:131], v[238:241], v[32:47]
	ds_read_b64_tr_b16 v[238:239], v174 offset:0x400
	ds_read_b64_tr_b16 v[240:241], v174 offset:0xc00
	v_sub_f32_e32 v198, v161, v160
	v_max_f32_e32 v161, v205, v161
	v_sub_f32_e32 v205, v160, v161
	v_mul_f32_e32 v205, 0x3dd53b94, v205
	v_exp_f32_e32 v205, v205
	v_mfma_f32_32x32x16_bf16 v[32:47], v[132:135], v[242:245], v[32:47]
	ds_read_b64_tr_b16 v[242:243], v174 offset:0x1400
	ds_read_b64_tr_b16 v[244:245], v174 offset:0x1c00
	v_cmp_ge_f32_e32 vcc, s48, v198
	s_cmp_eq_u64 vcc, exec
	s_cselect_b64 s[6:7], -1, 0
	v_cndmask_b32_e64 v205, v205, 1.0, s[6:7]
	v_cndmask_b32_e64 v198, v161, v160, s[6:7]
	v_mul_f32_e32 v236, 0xbdd53b94, v198
	v_mov_b32_e32 v237, v236
	v_cmp_gt_f32_e32 vcc, 1.0, v205
	v_mfma_f32_32x32x16_bf16 v[32:47], v[136:139], v[246:249], v[32:47]
	ds_read_b64_tr_b16 v[246:247], v174 offset:0x2400
	ds_read_b64_tr_b16 v[248:249], v174 offset:0x2c00
	ds_read_b64_tr_b16 v[250:251], v174 offset:0x3400
	ds_read_b64_tr_b16 v[252:253], v174 offset:0x3c00
	v_fmamk_f32 v80, v80, 0x3dd53b94, v236
	v_fmamk_f32 v81, v81, 0x3dd53b94, v236
	v_fmamk_f32 v82, v82, 0x3dd53b94, v236
	v_fmamk_f32 v83, v83, 0x3dd53b94, v236
	v_mfma_f32_32x32x16_bf16 v[32:47], v[208:211], v[162:165], v[32:47]
	v_fmamk_f32 v84, v84, 0x3dd53b94, v236
	v_fmamk_f32 v85, v85, 0x3dd53b94, v236
	v_fmamk_f32 v86, v86, 0x3dd53b94, v236
	v_fmamk_f32 v87, v87, 0x3dd53b94, v236
	s_waitcnt lgkmcnt(0)
	v_mfma_f32_32x32x16_bf16 v[0:15], v[128:131], v[238:241], v[0:15]
	ds_read_b64_tr_b16 v[162:163], v174 offset:0x600
	ds_read_b64_tr_b16 v[164:165], v174 offset:0xe00
	ds_read_b64_tr_b16 v[238:239], v174 offset:0x1600
	ds_read_b64_tr_b16 v[240:241], v174 offset:0x1e00
	v_fmamk_f32 v88, v88, 0x3dd53b94, v236
	v_fmamk_f32 v89, v89, 0x3dd53b94, v236
	v_fmamk_f32 v90, v90, 0x3dd53b94, v236
	v_fmamk_f32 v91, v91, 0x3dd53b94, v236
	v_mfma_f32_32x32x16_bf16 v[0:15], v[132:135], v[242:245], v[0:15]
	ds_read_b64_tr_b16 v[242:243], v174 offset:0x2600
	ds_read_b64_tr_b16 v[244:245], v174 offset:0x2e00
	v_fmamk_f32 v92, v92, 0x3dd53b94, v236
	v_fmamk_f32 v93, v93, 0x3dd53b94, v236
	v_fmamk_f32 v94, v94, 0x3dd53b94, v236
	v_fmamk_f32 v95, v95, 0x3dd53b94, v236
	v_mfma_f32_32x32x16_bf16 v[0:15], v[136:139], v[246:249], v[0:15]
	ds_read_b64_tr_b16 v[246:247], v174 offset:0x3600
	ds_read_b64_tr_b16 v[248:249], v174 offset:0x3e00
	v_exp_f32_e32 v222, v80
	v_exp_f32_e32 v224, v81
	v_exp_f32_e32 v220, v82
	v_mfma_f32_32x32x16_bf16 v[0:15], v[208:211], v[250:253], v[0:15]
	v_exp_f32_e32 v223, v83
	v_exp_f32_e32 v219, v84
	v_exp_f32_e32 v221, v85
	s_waitcnt lgkmcnt(0)
	v_mfma_f32_32x32x16_bf16 v[48:63], v[128:131], v[162:165], v[48:63]
	v_exp_f32_e32 v217, v86
	v_exp_f32_e32 v218, v87
	v_exp_f32_e32 v212, v88
	v_pk_fma_f32 v[130:131], v[70:71], s[28:29], v[236:237] op_sel_hi:[1,0,0]
	v_pk_fma_f32 v[128:129], v[72:73], s[28:29], v[236:237] op_sel_hi:[1,0,0]
	v_mfma_f32_32x32x16_bf16 v[48:63], v[132:135], v[238:241], v[48:63]
	v_exp_f32_e32 v214, v89
	v_exp_f32_e32 v213, v91
	v_exp_f32_e32 v207, v94
	v_pk_fma_f32 v[132:133], v[68:69], s[28:29], v[236:237] op_sel_hi:[1,0,0]
	v_pk_fma_f32 v[134:135], v[78:79], s[28:29], v[236:237] op_sel_hi:[1,0,0]
	v_mfma_f32_32x32x16_bf16 v[48:63], v[136:139], v[242:245], v[48:63]
	v_pk_fma_f32 v[138:139], v[64:65], s[28:29], v[236:237] op_sel_hi:[1,0,0]
	v_pk_fma_f32 v[136:137], v[66:67], s[28:29], v[236:237] op_sel_hi:[1,0,0]
	v_pk_fma_f32 v[162:163], v[74:75], s[28:29], v[236:237] op_sel_hi:[1,0,0]
	v_pk_fma_f32 v[160:161], v[76:77], s[28:29], v[236:237] op_sel_hi:[1,0,0]
	v_mfma_f32_32x32x16_bf16 v[48:63], v[208:211], v[246:249], v[48:63]
	v_exp_f32_e32 v211, v90
	v_exp_f32_e32 v208, v92
	v_exp_f32_e32 v210, v93
	v_exp_f32_e32 v209, v95
	v_add_f32_e32 v64, v203, v204
	v_fmac_f32_e32 v64, v197, v140
	v_add_f32_e32 v140, v215, v216
	s_addk_i32 s10, 0x80
	s_add_i32 s64, s64, 2
	s_addk_i32 s11, 0x80
	v_fmac_f32_e32 v140, v64, v206
	s_cbranch_vccz .LBB0_765
	s_and_saveexec_b64 s[8:9], s[4:5]
	ds_write_b32 v189, v205 offset:128
	s_or_b64 exec, exec, s[8:9]
	s_waitcnt lgkmcnt(0)
	v_add_u32_e32 v164, s62, v169
	ds_read_b128 v[238:241], v164 offset:224
	ds_read_b128 v[242:245], v164 offset:192
	ds_read_b128 v[246:249], v164 offset:160
	ds_read_b128 v[250:253], v164 offset:128
	s_waitcnt lgkmcnt(3)
	v_pk_mul_f32 v[28:29], v[28:29], v[238:239]
	s_waitcnt lgkmcnt(2)
	v_pk_mul_f32 v[24:25], v[24:25], v[242:243]
	s_waitcnt lgkmcnt(1)
	v_pk_mul_f32 v[20:21], v[20:21], v[246:247]
	v_pk_mul_f32 v[30:31], v[30:31], v[240:241]
	v_pk_mul_f32 v[26:27], v[26:27], v[244:245]
	v_pk_mul_f32 v[22:23], v[22:23], v[248:249]
	s_waitcnt lgkmcnt(0)
	v_pk_mul_f32 v[18:19], v[18:19], v[252:253]
	v_pk_mul_f32 v[16:17], v[16:17], v[250:251]
	v_pk_mul_f32 v[44:45], v[44:45], v[238:239]
	v_pk_mul_f32 v[40:41], v[40:41], v[242:243]
	v_pk_mul_f32 v[36:37], v[36:37], v[246:247]
	v_pk_mul_f32 v[46:47], v[46:47], v[240:241]
	v_pk_mul_f32 v[42:43], v[42:43], v[244:245]
	v_pk_mul_f32 v[38:39], v[38:39], v[248:249]
	v_pk_mul_f32 v[34:35], v[34:35], v[252:253]
	v_pk_mul_f32 v[32:33], v[32:33], v[250:251]
	v_pk_mul_f32 v[12:13], v[12:13], v[238:239]
	v_pk_mul_f32 v[8:9], v[8:9], v[242:243]
	v_pk_mul_f32 v[4:5], v[4:5], v[246:247]
	v_pk_mul_f32 v[14:15], v[14:15], v[240:241]
	v_pk_mul_f32 v[10:11], v[10:11], v[244:245]
	v_pk_mul_f32 v[6:7], v[6:7], v[248:249]
	v_pk_mul_f32 v[2:3], v[2:3], v[252:253]
	v_pk_mul_f32 v[0:1], v[0:1], v[250:251]
	v_pk_mul_f32 v[60:61], v[60:61], v[238:239]
	v_pk_mul_f32 v[56:57], v[56:57], v[242:243]
	v_pk_mul_f32 v[52:53], v[52:53], v[246:247]
	v_pk_mul_f32 v[62:63], v[62:63], v[240:241]
	v_pk_mul_f32 v[58:59], v[58:59], v[244:245]
	v_pk_mul_f32 v[54:55], v[54:55], v[248:249]
	v_pk_mul_f32 v[50:51], v[50:51], v[252:253]
	v_pk_mul_f32 v[48:49], v[48:49], v[250:251]

.LBB0_2012:
	ds_read_b128 v[64:67], v180 offset:49152
	ds_read_b128 v[68:71], v180 offset:57344
	ds_read_b128 v[200:203], v181 offset:49152
	ds_read_b128 v[226:229], v181 offset:57344
	ds_read_b128 v[230:233], v182 offset:49152
	ds_read_b128 v[234:237], v182 offset:57344
	ds_read_b128 v[238:241], v183 offset:49152
	ds_read_b128 v[242:245], v183 offset:57344
	s_add_i32 s6, 0, 0x12000
	v_add_u32_e32 v199, s6, v170
	v_add_u32_e32 v204, s6, v171
	v_add_u32_e32 v205, s6, v172
	s_waitcnt lgkmcnt(7)
	v_mfma_f32_32x32x16_bf16 v[80:95], v[64:67], v[124:127], 0
	s_add_i32 s8, s8, 2
	s_sub_i32 s80, s14, 64
	s_cmp_lt_u32 s8, 3
	s_cselect_b32 s80, s13, s80
	s_mul_i32 s81, s80, 0xc00
	s_add_i32 s85, s82, 0x8000
	s_mov_b32 m0, s85
	s_add_i32 s85, s82, 0x10000
	buffer_load_dwordx4 v154, s[72:75], s81 offen lds
	v_exp_f32_e32 v216, v128
	v_add_f32_e32 v128, 0, v222
	v_add_f32_e32 v128, v224, v128
	v_add_f32_e32 v128, v220, v128
	v_add_f32_e32 v128, v223, v128
	v_add_f32_e32 v128, v219, v128
	v_add_f32_e32 v128, v221, v128
	s_waitcnt lgkmcnt(6)
	v_mfma_f32_32x32x16_bf16 v[64:79], v[68:71], v[124:127], 0
	s_mov_b32 m0, s85
	s_add_i32 s85, s82, 0xa000
	buffer_load_dwordx4 v155, s[72:75], s81 offen lds
	v_add_f32_e32 v128, v217, v128
	v_add_f32_e32 v128, v218, v128
	v_add_f32_e32 v128, v212, v128
	v_add_f32_e32 v128, v214, v128
	v_add_f32_e32 v128, v211, v128
	v_add_f32_e32 v128, v213, v128
	v_exp_f32_e32 v138, v138
	s_waitcnt lgkmcnt(5)
	v_mfma_f32_32x32x16_bf16 v[80:95], v[200:203], v[120:123], v[80:95]
	s_mov_b32 m0, s85
	s_add_i32 s81, s81, 0x18000
	buffer_load_dwordx4 v154, s[72:75], s81 offen lds
	v_add_f32_e32 v128, v208, v128
	v_exp_f32_e32 v139, v139
	v_add_f32_e32 v128, v210, v128
	v_exp_f32_e32 v164, v136
	v_add_f32_e32 v128, v207, v128
	v_exp_f32_e32 v137, v137
	v_add_f32_e32 v128, v209, v128
	s_waitcnt lgkmcnt(4)
	v_mfma_f32_32x32x16_bf16 v[64:79], v[226:229], v[120:123], v[64:79]
	s_lshl_b32 s81, s83, 11
	s_add_i32 s85, s82, 0x4000
	s_mov_b32 m0, s85
	s_add_i32 s85, s82, 0x6000
	buffer_load_dwordx4 v196, s[76:79], s81 offen lds
	ds_read_b128 v[200:203], v184 offset:49152
	ds_read_b128 v[226:229], v184 offset:57344
	v_exp_f32_e32 v165, v132
	v_add_f32_e32 v128, v138, v128
	v_add_f32_e32 v128, v139, v128
	v_exp_f32_e32 v206, v130
	v_add_f32_e32 v128, v164, v128
	v_exp_f32_e32 v215, v131
	s_waitcnt lgkmcnt(5)
	v_mfma_f32_32x32x16_bf16 v[80:95], v[230:233], v[116:119], v[80:95]
	s_mov_b32 m0, s85
	s_add_i32 s81, s81, 0x10000
	buffer_load_dwordx4 v196, s[76:79], s81 offen lds
	s_mov_b32 s84, s80
	v_add_f32_e32 v128, v137, v128
	v_add_f32_e32 v128, v165, v128
	v_exp_f32_e32 v225, v129
	v_exp_f32_e32 v162, v162
	v_exp_f32_e32 v163, v163
	v_exp_f32_e32 v160, v160
	v_exp_f32_e32 v161, v161
	s_waitcnt lgkmcnt(4)
	v_mfma_f32_32x32x16_bf16 v[64:79], v[234:237], v[116:119], v[64:79]
	ds_read_b128 v[230:233], v185 offset:49152
	ds_read_b128 v[234:237], v185 offset:57344
	v_cvt_pk_bf16_f32 v129, v220, v223
	v_cvt_pk_bf16_f32 v130, v219, v221
	v_cvt_pk_bf16_f32 v131, v217, v218
	v_cvt_pk_bf16_f32 v132, v212, v214
	v_cvt_pk_bf16_f32 v136, v138, v139
	v_cvt_pk_bf16_f32 v137, v164, v137
	s_waitcnt lgkmcnt(5)
	v_mfma_f32_32x32x16_bf16 v[80:95], v[238:241], v[112:115], v[80:95]
	v_cvt_pk_bf16_f32 v139, v206, v215
	v_permlane32_swap_b32_e32 v129, v131
	s_nop 0
	v_permlane32_swap_b32_e32 v137, v139
	s_waitcnt lgkmcnt(4)
	v_mfma_f32_32x32x16_bf16 v[64:79], v[242:245], v[112:115], v[64:79]
	ds_read_b128 v[238:241], v186 offset:49152
	ds_read_b128 v[242:245], v186 offset:57344
	s_waitcnt lgkmcnt(5)
	v_mfma_f32_32x32x16_bf16 v[80:95], v[200:203], v[108:111], v[80:95]
	s_waitcnt lgkmcnt(4)
	v_mfma_f32_32x32x16_bf16 v[64:79], v[226:229], v[108:111], v[64:79]
	ds_read_b128 v[200:203], v187 offset:49152
	ds_read_b128 v[226:229], v187 offset:57344
	s_waitcnt lgkmcnt(5)
	v_mfma_f32_32x32x16_bf16 v[80:95], v[230:233], v[104:107], v[80:95]
	s_waitcnt lgkmcnt(4)
	v_mfma_f32_32x32x16_bf16 v[64:79], v[234:237], v[104:107], v[64:79]
	ds_read_b128 v[230:233], v199
	ds_read_b128 v[234:237], v199 offset:4096
	s_waitcnt lgkmcnt(5)
	v_mfma_f32_32x32x16_bf16 v[80:95], v[238:241], v[100:103], v[80:95]
	s_waitcnt lgkmcnt(4)
	v_mfma_f32_32x32x16_bf16 v[64:79], v[242:245], v[100:103], v[64:79]
	ds_read_b128 v[238:241], v204
	ds_read_b128 v[242:245], v204 offset:4096
	v_add_u32_e32 v204, s6, v173
	s_waitcnt lgkmcnt(5)
	v_mfma_f32_32x32x16_bf16 v[80:95], v[200:203], v[96:99], v[80:95]
	s_waitcnt lgkmcnt(4)
	v_mfma_f32_32x32x16_bf16 v[64:79], v[226:229], v[96:99], v[64:79]
	ds_read_b128 v[200:203], v205
	ds_read_b128 v[226:229], v205 offset:4096
	s_waitcnt lgkmcnt(5)
	v_mfma_f32_32x32x16_bf16 v[80:95], v[230:233], v[142:145], v[80:95]
	s_waitcnt lgkmcnt(4)
	v_mfma_f32_32x32x16_bf16 v[64:79], v[234:237], v[142:145], v[64:79]
	ds_read_b128 v[230:233], v204
	ds_read_b128 v[234:237], v204 offset:4096
	s_waitcnt lgkmcnt(5)
	v_mfma_f32_32x32x16_bf16 v[80:95], v[238:241], v[146:149], v[80:95]
	s_waitcnt lgkmcnt(4)
	v_mfma_f32_32x32x16_bf16 v[64:79], v[242:245], v[146:149], v[64:79]
	s_waitcnt lgkmcnt(3)
	v_mfma_f32_32x32x16_bf16 v[80:95], v[200:203], v[150:153], v[80:95]
	v_exp_f32_e32 v205, v133
	v_cvt_pk_bf16_f32 v133, v211, v213
	v_cvt_pk_bf16_f32 v138, v165, v205
	v_add_f32_e32 v128, v205, v128
	v_add_f32_e32 v128, v206, v128
	v_add_f32_e32 v128, v215, v128
	s_waitcnt lgkmcnt(2)
	v_mfma_f32_32x32x16_bf16 v[64:79], v[226:229], v[150:153], v[64:79]
	v_add_f32_e32 v128, v216, v128
	v_add_f32_e32 v128, v225, v128
	v_add_f32_e32 v128, v162, v128
	v_add_f32_e32 v128, v163, v128
	v_add_f32_e32 v128, v160, v128
	v_add_f32_e32 v128, v161, v128
	s_waitcnt lgkmcnt(1)
	v_mfma_f32_32x32x16_bf16 v[80:95], v[230:233], v[156:159], v[80:95]
	v_exp_f32_e32 v226, v134
	v_exp_f32_e32 v227, v135
	v_cvt_pk_bf16_f32 v134, v208, v210
	v_cvt_pk_bf16_f32 v135, v207, v209
	v_add_f32_e32 v128, v226, v128
	v_add_f32_e32 v203, v227, v128
	v_mov_b32_e32 v204, v203
	s_waitcnt lgkmcnt(0)
	v_mfma_f32_32x32x16_bf16 v[64:79], v[234:237], v[156:159], v[64:79]
	s_nop 0
	v_permlane32_swap_b32_e32 v203, v204
	v_cvt_pk_bf16_f32 v128, v222, v224
	v_cvt_pk_bf16_f32 v208, v216, v225
	v_cvt_pk_bf16_f32 v209, v162, v163
	v_cvt_pk_bf16_f32 v210, v160, v161
	v_cvt_pk_bf16_f32 v211, v226, v227
	v_permlane32_swap_b32_e32 v132, v134
	v_permlane32_swap_b32_e32 v128, v130
	v_permlane32_swap_b32_e32 v133, v135
	v_permlane32_swap_b32_e32 v136, v138
	v_permlane32_swap_b32_e32 v208, v210
	v_permlane32_swap_b32_e32 v209, v211
	ds_read_b64_tr_b16 v[160:161], v167 offset:0
	ds_read_b64_tr_b16 v[162:163], v167 offset:0x800
	ds_read_b64_tr_b16 v[232:233], v167 offset:0x1000
	ds_read_b64_tr_b16 v[234:235], v167 offset:0x1800
	ds_read_b64_tr_b16 v[236:237], v167 offset:0x2000
	ds_read_b64_tr_b16 v[238:239], v167 offset:0x2800
	ds_read_b64_tr_b16 v[240:241], v167 offset:0x3000
	ds_read_b64_tr_b16 v[242:243], v167 offset:0x3800
	v_max_f32_e32 v164, v81, v81
	v_max_f32_e32 v165, v80, v80
	v_max_f32_e32 v164, v165, v164
	v_max3_f32 v164, v164, v82, v83
	v_max3_f32 v164, v164, v84, v85
	v_max3_f32 v164, v164, v86, v87
	v_max3_f32 v164, v164, v88, v89
	v_max3_f32 v164, v164, v90, v91
	v_max3_f32 v164, v164, v92, v93
	v_max3_f32 v164, v164, v94, v95
	s_waitcnt lgkmcnt(0)
	v_mfma_f32_32x32x16_bf16 v[0:15], v[128:131], v[160:163], v[0:15]
	v_max3_f32 v160, v164, v64, v65
	v_max3_f32 v160, v160, v66, v67
	v_max3_f32 v160, v160, v68, v69
	v_mfma_f32_32x32x16_bf16 v[0:15], v[132:135], v[232:235], v[0:15]
	ds_read_b64_tr_b16 v[232:233], v167 offset:0x200
	ds_read_b64_tr_b16 v[234:235], v167 offset:0xa00
	v_max3_f32 v160, v160, v70, v71
	v_max3_f32 v160, v160, v72, v73
	v_max3_f32 v160, v160, v74, v75
	v_mfma_f32_32x32x16_bf16 v[0:15], v[136:139], v[236:239], v[0:15]
	ds_read_b64_tr_b16 v[236:237], v167 offset:0x1200
	ds_read_b64_tr_b16 v[238:239], v167 offset:0x1a00
	ds_read_b64_tr_b16 v[244:245], v167 offset:0x2200
	ds_read_b64_tr_b16 v[246:247], v167 offset:0x2a00
	ds_read_b64_tr_b16 v[248:249], v167 offset:0x3200
	ds_read_b64_tr_b16 v[250:251], v167 offset:0x3a00
	v_max3_f32 v160, v160, v76, v77
	v_max3_f32 v160, v160, v78, v79
	v_mov_b32_e32 v161, v160
	v_mfma_f32_32x32x16_bf16 v[0:15], v[208:211], v[240:243], v[0:15]
	v_max_f32_e32 v162, v198, v198
	v_permlane32_swap_b32_e32 v160, v161
	v_max_f32_e32 v161, v161, v161
	v_max_f32_e32 v160, v160, v160
	v_max_f32_e32 v160, v160, v161
	s_waitcnt lgkmcnt(0)
	v_mfma_f32_32x32x16_bf16 v[32:47], v[128:131], v[232:235], v[32:47]
	ds_read_b64_tr_b16 v[232:233], v167 offset:0x400
	ds_read_b64_tr_b16 v[234:235], v167 offset:0xc00
	v_sub_f32_e32 v161, v160, v198
	v_max_f32_e32 v160, v162, v160
	v_sub_f32_e32 v162, v198, v160
	v_mul_f32_e32 v162, 0x3dd53b94, v162
	v_exp_f32_e32 v162, v162
	v_mfma_f32_32x32x16_bf16 v[32:47], v[132:135], v[236:239], v[32:47]
	ds_read_b64_tr_b16 v[236:237], v167 offset:0x1400
	ds_read_b64_tr_b16 v[238:239], v167 offset:0x1c00
	ds_read_b64_tr_b16 v[240:241], v167 offset:0x2400
	ds_read_b64_tr_b16 v[242:243], v167 offset:0x2c00
	v_cmp_ge_f32_e32 vcc, s46, v161
	s_cmp_eq_u64 vcc, exec
	s_cselect_b64 s[6:7], -1, 0
	v_cndmask_b32_e64 v206, v162, 1.0, s[6:7]
	v_cndmask_b32_e64 v160, v160, v198, s[6:7]
	v_mul_f32_e32 v205, 0xbdd53b94, v160
	v_cmp_gt_f32_e32 vcc, 1.0, v206
	v_mfma_f32_32x32x16_bf16 v[32:47], v[136:139], v[244:247], v[32:47]
	ds_read_b64_tr_b16 v[244:245], v167 offset:0x3400
	ds_read_b64_tr_b16 v[246:247], v167 offset:0x3c00
	v_fmamk_f32 v87, v87, 0x3dd53b94, v205
	v_fmamk_f32 v80, v80, 0x3dd53b94, v205
	v_fmamk_f32 v81, v81, 0x3dd53b94, v205
	v_fmamk_f32 v82, v82, 0x3dd53b94, v205
	v_fmamk_f32 v83, v83, 0x3dd53b94, v205
	v_mfma_f32_32x32x16_bf16 v[32:47], v[208:211], v[248:251], v[32:47]
	v_fmamk_f32 v84, v84, 0x3dd53b94, v205
	v_fmamk_f32 v85, v85, 0x3dd53b94, v205
	v_fmamk_f32 v86, v86, 0x3dd53b94, v205
	v_fmamk_f32 v88, v88, 0x3dd53b94, v205
	v_fmamk_f32 v89, v89, 0x3dd53b94, v205
	s_waitcnt lgkmcnt(0)
	v_mfma_f32_32x32x16_bf16 v[16:31], v[128:131], v[232:235], v[16:31]
	ds_read_b64_tr_b16 v[232:233], v167 offset:0x600
	ds_read_b64_tr_b16 v[234:235], v167 offset:0xe00
	v_fmamk_f32 v90, v90, 0x3dd53b94, v205
	v_fmamk_f32 v91, v91, 0x3dd53b94, v205
	v_fmamk_f32 v92, v92, 0x3dd53b94, v205
	v_fmamk_f32 v93, v93, 0x3dd53b94, v205
	v_fmamk_f32 v94, v94, 0x3dd53b94, v205
	v_mfma_f32_32x32x16_bf16 v[16:31], v[132:135], v[236:239], v[16:31]
	ds_read_b64_tr_b16 v[236:237], v167 offset:0x1600
	ds_read_b64_tr_b16 v[238:239], v167 offset:0x1e00
	v_fmamk_f32 v95, v95, 0x3dd53b94, v205
	v_fmamk_f32 v215, v64, 0x3dd53b94, v205
	v_fmamk_f32 v216, v65, 0x3dd53b94, v205
	v_fmamk_f32 v217, v66, 0x3dd53b94, v205
	v_fmamk_f32 v218, v67, 0x3dd53b94, v205
	v_mfma_f32_32x32x16_bf16 v[16:31], v[136:139], v[240:243], v[16:31]
	ds_read_b64_tr_b16 v[240:241], v167 offset:0x2600
	ds_read_b64_tr_b16 v[242:243], v167 offset:0x2e00
	ds_read_b64_tr_b16 v[248:249], v167 offset:0x3600
	ds_read_b64_tr_b16 v[250:251], v167 offset:0x3e00
	v_fmamk_f32 v219, v68, 0x3dd53b94, v205
	v_fmamk_f32 v212, v73, 0x3dd53b94, v205
	v_fmamk_f32 v213, v74, 0x3dd53b94, v205
	v_fmamk_f32 v214, v75, 0x3dd53b94, v205
	v_mfma_f32_32x32x16_bf16 v[16:31], v[208:211], v[244:247], v[16:31]
	v_fmamk_f32 v207, v76, 0x3dd53b94, v205
	v_fmamk_f32 v220, v77, 0x3dd53b94, v205
	v_fmamk_f32 v221, v78, 0x3dd53b94, v205
	s_waitcnt lgkmcnt(0)
	v_mfma_f32_32x32x16_bf16 v[48:63], v[128:131], v[232:235], v[48:63]
	v_exp_f32_e32 v128, v80
	v_exp_f32_e32 v129, v82
	v_exp_f32_e32 v130, v84
	v_exp_f32_e32 v131, v86
	v_mfma_f32_32x32x16_bf16 v[48:63], v[132:135], v[236:239], v[48:63]
	v_exp_f32_e32 v132, v88
	v_exp_f32_e32 v133, v90
	v_exp_f32_e32 v134, v92
	v_exp_f32_e32 v135, v94
	v_mfma_f32_32x32x16_bf16 v[48:63], v[136:139], v[240:243], v[48:63]
	v_exp_f32_e32 v139, v89
	v_exp_f32_e32 v138, v91
	v_exp_f32_e32 v137, v93
	v_exp_f32_e32 v136, v95
	v_mfma_f32_32x32x16_bf16 v[48:63], v[208:211], v[248:251], v[48:63]
	v_exp_f32_e32 v161, v87
	v_exp_f32_e32 v198, v81
	v_exp_f32_e32 v163, v83
	v_exp_f32_e32 v162, v85
	v_fmamk_f32 v208, v69, 0x3dd53b94, v205
	v_fmamk_f32 v209, v70, 0x3dd53b94, v205
	v_fmamk_f32 v210, v71, 0x3dd53b94, v205
	v_fmamk_f32 v211, v72, 0x3dd53b94, v205
	v_fmac_f32_e32 v205, 0x3dd53b94, v79
	s_cbranch_vccz .LBB0_2016
	s_and_saveexec_b64 s[10:11], s[4:5]
	ds_write_b32 v189, v206 offset:128
	s_or_b64 exec, exec, s[10:11]
	s_waitcnt lgkmcnt(0)
	v_add_u32_e32 v248, s12, v169
	ds_read_b128 v[232:235], v248 offset:224
	ds_read_b128 v[236:239], v248 offset:192
	ds_read_b128 v[240:243], v248 offset:160
	ds_read_b128 v[244:247], v248 offset:128
	s_waitcnt lgkmcnt(3)
	v_pk_mul_f32 v[12:13], v[12:13], v[232:233]
	s_waitcnt lgkmcnt(2)
	v_pk_mul_f32 v[8:9], v[8:9], v[236:237]
	s_waitcnt lgkmcnt(1)
	v_pk_mul_f32 v[4:5], v[4:5], v[240:241]
	v_pk_mul_f32 v[14:15], v[14:15], v[234:235]
	v_pk_mul_f32 v[10:11], v[10:11], v[238:239]
	v_pk_mul_f32 v[6:7], v[6:7], v[242:243]
	s_waitcnt lgkmcnt(0)
	v_pk_mul_f32 v[2:3], v[2:3], v[246:247]
	v_pk_mul_f32 v[0:1], v[0:1], v[244:245]
	v_pk_mul_f32 v[44:45], v[44:45], v[232:233]
	v_pk_mul_f32 v[40:41], v[40:41], v[236:237]
	v_pk_mul_f32 v[36:37], v[36:37], v[240:241]
	v_pk_mul_f32 v[46:47], v[46:47], v[234:235]
	v_pk_mul_f32 v[42:43], v[42:43], v[238:239]
	v_pk_mul_f32 v[38:39], v[38:39], v[242:243]
	v_pk_mul_f32 v[34:35], v[34:35], v[246:247]
	v_pk_mul_f32 v[32:33], v[32:33], v[244:245]
	v_pk_mul_f32 v[28:29], v[28:29], v[232:233]
	v_pk_mul_f32 v[24:25], v[24:25], v[236:237]
	v_pk_mul_f32 v[20:21], v[20:21], v[240:241]
	v_pk_mul_f32 v[30:31], v[30:31], v[234:235]
	v_pk_mul_f32 v[26:27], v[26:27], v[238:239]
	v_pk_mul_f32 v[22:23], v[22:23], v[242:243]
	v_pk_mul_f32 v[18:19], v[18:19], v[246:247]
	v_pk_mul_f32 v[16:17], v[16:17], v[244:245]
	v_pk_mul_f32 v[60:61], v[60:61], v[232:233]
	v_pk_mul_f32 v[56:57], v[56:57], v[236:237]
	v_pk_mul_f32 v[52:53], v[52:53], v[240:241]
	v_pk_mul_f32 v[62:63], v[62:63], v[234:235]
	v_pk_mul_f32 v[58:59], v[58:59], v[238:239]
	v_pk_mul_f32 v[54:55], v[54:55], v[242:243]
	v_pk_mul_f32 v[50:51], v[50:51], v[246:247]
	v_pk_mul_f32 v[48:49], v[48:49], v[244:245]
.LBB0_2016:
	s_waitcnt vmcnt(0) lgkmcnt(0)
	s_barrier
	ds_read_b128 v[64:67], v180 offset:32768
	ds_read_b128 v[68:71], v180 offset:40960
	ds_read_b128 v[222:225], v181 offset:32768
	ds_read_b128 v[226:229], v181 offset:40960
	ds_read_b128 v[230:233], v182 offset:32768
	ds_read_b128 v[234:237], v182 offset:40960
	ds_read_b128 v[238:241], v183 offset:32768
	ds_read_b128 v[242:245], v183 offset:40960
	v_exp_f32_e32 v164, v215
	v_add_f32_e32 v215, 0, v128
	s_waitcnt lgkmcnt(7)
	v_mfma_f32_32x32x16_bf16 v[80:95], v[64:67], v[124:127], 0
	s_add_i32 s80, s13, 64
	s_cmp_lt_u32 s8, 2
	s_cselect_b32 s80, s80, s14
	s_mul_i32 s81, s80, 0xc00
	s_add_i32 s85, s82, 0xc000
	s_mov_b32 m0, s85
	s_add_i32 s85, s82, 0x12000
	buffer_load_dwordx4 v154, s[72:75], s81 offen lds
	v_add_f32_e32 v215, v198, v215
	v_add_f32_e32 v215, v129, v215
	v_add_f32_e32 v215, v163, v215
	v_add_f32_e32 v215, v130, v215
	v_add_f32_e32 v215, v162, v215
	v_add_f32_e32 v215, v131, v215
	v_add_f32_e32 v215, v161, v215
	s_waitcnt lgkmcnt(6)
	v_mfma_f32_32x32x16_bf16 v[64:79], v[68:71], v[124:127], 0
	s_mov_b32 m0, s85
	s_add_i32 s85, s82, 0xe000
	buffer_load_dwordx4 v155, s[72:75], s81 offen lds
	v_add_f32_e32 v215, v132, v215
	v_add_f32_e32 v215, v139, v215
	v_add_f32_e32 v215, v133, v215
	v_add_f32_e32 v215, v138, v215
	v_add_f32_e32 v215, v134, v215
	v_exp_f32_e32 v165, v216
	v_add_f32_e32 v215, v137, v215
	s_waitcnt lgkmcnt(5)
	v_mfma_f32_32x32x16_bf16 v[80:95], v[222:225], v[120:123], v[80:95]
	s_mov_b32 m0, s85
	s_add_i32 s81, s81, 0x18000
	buffer_load_dwordx4 v154, s[72:75], s81 offen lds
	v_exp_f32_e32 v217, v217
	v_add_f32_e32 v215, v135, v215
	v_exp_f32_e32 v218, v218
	v_add_f32_e32 v215, v136, v215
	v_exp_f32_e32 v219, v219
	v_add_f32_e32 v215, v164, v215
	v_exp_f32_e32 v208, v208
	s_waitcnt lgkmcnt(4)
	v_mfma_f32_32x32x16_bf16 v[64:79], v[226:229], v[120:123], v[64:79]
	s_lshl_b32 s81, s84, 11
	s_add_i32 s85, s82, 0x0
	s_mov_b32 m0, s85
	s_add_i32 s85, s82, 0x2000
	buffer_load_dwordx4 v196, s[76:79], s81 offen lds
	ds_read_b128 v[222:225], v184 offset:32768
	ds_read_b128 v[226:229], v184 offset:40960
	v_add_f32_e32 v215, v165, v215
	v_exp_f32_e32 v209, v209
	v_add_f32_e32 v215, v217, v215
	v_exp_f32_e32 v210, v210
	v_add_f32_e32 v215, v218, v215
	v_exp_f32_e32 v211, v211
	s_waitcnt lgkmcnt(5)
	v_mfma_f32_32x32x16_bf16 v[80:95], v[230:233], v[116:119], v[80:95]
	s_mov_b32 m0, s85
	s_add_i32 s81, s81, 0x10000
	buffer_load_dwordx4 v196, s[76:79], s81 offen lds
	s_mov_b32 s83, s80
	v_add_f32_e32 v215, v219, v215
	v_exp_f32_e32 v212, v212
	v_add_f32_e32 v215, v208, v215
	v_exp_f32_e32 v213, v213
	v_add_f32_e32 v215, v209, v215
	v_exp_f32_e32 v214, v214
	v_add_f32_e32 v215, v210, v215
	s_waitcnt lgkmcnt(4)
	v_mfma_f32_32x32x16_bf16 v[64:79], v[234:237], v[116:119], v[64:79]
	ds_read_b128 v[230:233], v185 offset:32768
	ds_read_b128 v[234:237], v185 offset:40960
	v_exp_f32_e32 v207, v207
	v_add_f32_e32 v215, v211, v215
	v_exp_f32_e32 v220, v220
	v_add_f32_e32 v215, v212, v215
	v_exp_f32_e32 v221, v221
	v_add_f32_e32 v215, v213, v215
	s_waitcnt lgkmcnt(5)
	v_mfma_f32_32x32x16_bf16 v[80:95], v[238:241], v[112:115], v[80:95]
	v_exp_f32_e32 v205, v205
	v_add_f32_e32 v215, v214, v215
	v_add_f32_e32 v215, v207, v215
	v_add_f32_e32 v215, v220, v215
	v_add_f32_e32 v215, v221, v215
	v_add_f32_e32 v215, v205, v215
	v_mov_b32_e32 v216, v215
	s_waitcnt lgkmcnt(4)
	v_mfma_f32_32x32x16_bf16 v[64:79], v[242:245], v[112:115], v[64:79]
	ds_read_b128 v[238:241], v186 offset:32768
	ds_read_b128 v[242:245], v186 offset:40960
	v_permlane32_swap_b32_e32 v215, v216
	v_cvt_pk_bf16_f32 v128, v128, v198
	v_cvt_pk_bf16_f32 v129, v129, v163
	v_cvt_pk_bf16_f32 v130, v130, v162
	v_cvt_pk_bf16_f32 v131, v131, v161
	s_waitcnt lgkmcnt(5)
	v_mfma_f32_32x32x16_bf16 v[80:95], v[222:225], v[108:111], v[80:95]
	v_cvt_pk_bf16_f32 v132, v132, v139
	v_cvt_pk_bf16_f32 v133, v133, v138
	v_cvt_pk_bf16_f32 v134, v134, v137
	v_cvt_pk_bf16_f32 v135, v135, v136
	v_cvt_pk_bf16_f32 v136, v164, v165
	v_cvt_pk_bf16_f32 v137, v217, v218
	v_cvt_pk_bf16_f32 v138, v219, v208
	s_waitcnt lgkmcnt(4)
	v_mfma_f32_32x32x16_bf16 v[64:79], v[226:229], v[108:111], v[64:79]
	ds_read_b128 v[222:225], v187 offset:32768
	ds_read_b128 v[226:229], v187 offset:40960
	v_cvt_pk_bf16_f32 v139, v209, v210
	v_cvt_pk_bf16_f32 v208, v211, v212
	v_cvt_pk_bf16_f32 v209, v213, v214
	v_cvt_pk_bf16_f32 v210, v207, v220
	v_cvt_pk_bf16_f32 v211, v221, v205
	v_permlane32_swap_b32_e32 v128, v130
	s_waitcnt lgkmcnt(5)
	v_mfma_f32_32x32x16_bf16 v[80:95], v[230:233], v[104:107], v[80:95]
	v_permlane32_swap_b32_e32 v129, v131
	v_permlane32_swap_b32_e32 v132, v134
	v_permlane32_swap_b32_e32 v133, v135
	v_permlane32_swap_b32_e32 v136, v138
	s_waitcnt lgkmcnt(4)
	v_mfma_f32_32x32x16_bf16 v[64:79], v[234:237], v[104:107], v[64:79]
	ds_read_b128 v[230:233], v191
	ds_read_b128 v[234:237], v191 offset:4096
	v_permlane32_swap_b32_e32 v137, v139
	v_permlane32_swap_b32_e32 v208, v210
	v_permlane32_swap_b32_e32 v209, v211
	s_waitcnt lgkmcnt(5)
	v_mfma_f32_32x32x16_bf16 v[80:95], v[238:241], v[100:103], v[80:95]
	s_waitcnt lgkmcnt(4)
	v_mfma_f32_32x32x16_bf16 v[64:79], v[242:245], v[100:103], v[64:79]
	ds_read_b128 v[238:241], v192
	ds_read_b128 v[242:245], v192 offset:4096
	s_waitcnt lgkmcnt(5)
	v_mfma_f32_32x32x16_bf16 v[80:95], v[222:225], v[96:99], v[80:95]
	s_waitcnt lgkmcnt(4)
	v_mfma_f32_32x32x16_bf16 v[64:79], v[226:229], v[96:99], v[64:79]
	ds_read_b128 v[222:225], v193
	ds_read_b128 v[226:229], v193 offset:4096
	s_waitcnt lgkmcnt(5)
	v_mfma_f32_32x32x16_bf16 v[80:95], v[230:233], v[142:145], v[80:95]
	s_waitcnt lgkmcnt(4)
	v_mfma_f32_32x32x16_bf16 v[64:79], v[234:237], v[142:145], v[64:79]
	ds_read_b128 v[230:233], v194
	ds_read_b128 v[234:237], v194 offset:4096
	s_waitcnt lgkmcnt(5)
	v_mfma_f32_32x32x16_bf16 v[80:95], v[238:241], v[146:149], v[80:95]
	s_waitcnt lgkmcnt(4)
	v_mfma_f32_32x32x16_bf16 v[64:79], v[242:245], v[146:149], v[64:79]
	s_waitcnt lgkmcnt(3)
	v_mfma_f32_32x32x16_bf16 v[80:95], v[222:225], v[150:153], v[80:95]
	s_waitcnt lgkmcnt(2)
	v_mfma_f32_32x32x16_bf16 v[64:79], v[226:229], v[150:153], v[64:79]
	s_waitcnt lgkmcnt(1)
	v_mfma_f32_32x32x16_bf16 v[80:95], v[230:233], v[156:159], v[80:95]
	s_waitcnt lgkmcnt(0)
	v_mfma_f32_32x32x16_bf16 v[64:79], v[234:237], v[156:159], v[64:79]
	ds_read_b64_tr_b16 v[238:239], v174 offset:0
	ds_read_b64_tr_b16 v[240:241], v174 offset:0x800
	ds_read_b64_tr_b16 v[242:243], v174 offset:0x1000
	ds_read_b64_tr_b16 v[244:245], v174 offset:0x1800
	ds_read_b64_tr_b16 v[246:247], v174 offset:0x2000
	ds_read_b64_tr_b16 v[248:249], v174 offset:0x2800
	ds_read_b64_tr_b16 v[250:251], v174 offset:0x3000
	ds_read_b64_tr_b16 v[252:253], v174 offset:0x3800
	s_nop 3
	v_max_f32_e32 v161, v81, v81
	v_max_f32_e32 v162, v80, v80
	v_max_f32_e32 v161, v162, v161
	v_max3_f32 v161, v161, v82, v83
	v_max3_f32 v161, v161, v84, v85
	v_max3_f32 v161, v161, v86, v87
	v_max3_f32 v161, v161, v88, v89
	v_max3_f32 v161, v161, v90, v91
	v_max3_f32 v161, v161, v92, v93
	v_max3_f32 v161, v161, v94, v95
	s_waitcnt lgkmcnt(0)
	v_mfma_f32_32x32x16_bf16 v[0:15], v[128:131], v[238:241], v[0:15]
	ds_read_b64_tr_b16 v[238:239], v174 offset:0x200
	ds_read_b64_tr_b16 v[240:241], v174 offset:0xa00
	v_max3_f32 v161, v161, v64, v65
	v_max3_f32 v161, v161, v66, v67
	v_max3_f32 v161, v161, v68, v69
	v_mfma_f32_32x32x16_bf16 v[0:15], v[132:135], v[242:245], v[0:15]
	ds_read_b64_tr_b16 v[242:243], v174 offset:0x1200
	ds_read_b64_tr_b16 v[244:245], v174 offset:0x1a00
	v_max3_f32 v161, v161, v70, v71
	v_max3_f32 v161, v161, v72, v73
	v_max3_f32 v161, v161, v74, v75
	v_mfma_f32_32x32x16_bf16 v[0:15], v[136:139], v[246:249], v[0:15]
	ds_read_b64_tr_b16 v[246:247], v174 offset:0x2200
	ds_read_b64_tr_b16 v[248:249], v174 offset:0x2a00
	ds_read_b64_tr_b16 v[162:163], v174 offset:0x3200
	ds_read_b64_tr_b16 v[164:165], v174 offset:0x3a00
	v_max3_f32 v161, v161, v76, v77
	v_max3_f32 v161, v161, v78, v79
	v_mov_b32_e32 v198, v161
	v_mfma_f32_32x32x16_bf16 v[0:15], v[208:211], v[250:253], v[0:15]
	v_max_f32_e32 v205, v160, v160
	v_permlane32_swap_b32_e32 v161, v198
	v_max_f32_e32 v198, v198, v198
	v_max_f32_e32 v161, v161, v161
	v_max_f32_e32 v161, v161, v198
	s_waitcnt lgkmcnt(0)
	v_mfma_f32_32x32x16_bf16 v[32:47], v[128:131], v[238:241], v[32:47]
	ds_read_b64_tr_b16 v[238:239], v174 offset:0x400
	ds_read_b64_tr_b16 v[240:241], v174 offset:0xc00
	v_sub_f32_e32 v198, v161, v160
	v_max_f32_e32 v161, v205, v161
	v_sub_f32_e32 v205, v160, v161
	v_mul_f32_e32 v205, 0x3dd53b94, v205
	v_exp_f32_e32 v205, v205
	v_mfma_f32_32x32x16_bf16 v[32:47], v[132:135], v[242:245], v[32:47]
	ds_read_b64_tr_b16 v[242:243], v174 offset:0x1400
	ds_read_b64_tr_b16 v[244:245], v174 offset:0x1c00
	v_cmp_ge_f32_e32 vcc, s46, v198
	s_cmp_eq_u64 vcc, exec
	s_cselect_b64 s[6:7], -1, 0
	v_cndmask_b32_e64 v205, v205, 1.0, s[6:7]
	v_cndmask_b32_e64 v198, v161, v160, s[6:7]
	v_mul_f32_e32 v236, 0xbdd53b94, v198
	v_mov_b32_e32 v237, v236
	v_cmp_gt_f32_e32 vcc, 1.0, v205
	v_mfma_f32_32x32x16_bf16 v[32:47], v[136:139], v[246:249], v[32:47]
	ds_read_b64_tr_b16 v[246:247], v174 offset:0x2400
	ds_read_b64_tr_b16 v[248:249], v174 offset:0x2c00
	ds_read_b64_tr_b16 v[250:251], v174 offset:0x3400
	ds_read_b64_tr_b16 v[252:253], v174 offset:0x3c00
	v_fmamk_f32 v80, v80, 0x3dd53b94, v236
	v_fmamk_f32 v81, v81, 0x3dd53b94, v236
	v_fmamk_f32 v82, v82, 0x3dd53b94, v236
	v_fmamk_f32 v83, v83, 0x3dd53b94, v236
	v_mfma_f32_32x32x16_bf16 v[32:47], v[208:211], v[162:165], v[32:47]
	v_fmamk_f32 v84, v84, 0x3dd53b94, v236
	v_fmamk_f32 v85, v85, 0x3dd53b94, v236
	v_fmamk_f32 v86, v86, 0x3dd53b94, v236
	v_fmamk_f32 v87, v87, 0x3dd53b94, v236
	s_waitcnt lgkmcnt(0)
	v_mfma_f32_32x32x16_bf16 v[16:31], v[128:131], v[238:241], v[16:31]
	ds_read_b64_tr_b16 v[162:163], v174 offset:0x600
	ds_read_b64_tr_b16 v[164:165], v174 offset:0xe00
	ds_read_b64_tr_b16 v[238:239], v174 offset:0x1600
	ds_read_b64_tr_b16 v[240:241], v174 offset:0x1e00
	v_fmamk_f32 v88, v88, 0x3dd53b94, v236
	v_fmamk_f32 v89, v89, 0x3dd53b94, v236
	v_fmamk_f32 v90, v90, 0x3dd53b94, v236
	v_fmamk_f32 v91, v91, 0x3dd53b94, v236
	v_mfma_f32_32x32x16_bf16 v[16:31], v[132:135], v[242:245], v[16:31]
	ds_read_b64_tr_b16 v[242:243], v174 offset:0x2600
	ds_read_b64_tr_b16 v[244:245], v174 offset:0x2e00
	v_fmamk_f32 v92, v92, 0x3dd53b94, v236
	v_fmamk_f32 v93, v93, 0x3dd53b94, v236
	v_fmamk_f32 v94, v94, 0x3dd53b94, v236
	v_fmamk_f32 v95, v95, 0x3dd53b94, v236
	v_mfma_f32_32x32x16_bf16 v[16:31], v[136:139], v[246:249], v[16:31]
	ds_read_b64_tr_b16 v[246:247], v174 offset:0x3600
	ds_read_b64_tr_b16 v[248:249], v174 offset:0x3e00
	v_exp_f32_e32 v222, v80
	v_exp_f32_e32 v224, v81
	v_exp_f32_e32 v220, v82
	v_mfma_f32_32x32x16_bf16 v[16:31], v[208:211], v[250:253], v[16:31]
	v_exp_f32_e32 v223, v83
	v_exp_f32_e32 v219, v84
	v_exp_f32_e32 v221, v85
	s_waitcnt lgkmcnt(0)
	v_mfma_f32_32x32x16_bf16 v[48:63], v[128:131], v[162:165], v[48:63]
	v_exp_f32_e32 v217, v86
	v_exp_f32_e32 v218, v87
	v_exp_f32_e32 v212, v88
	v_pk_fma_f32 v[130:131], v[70:71], s[26:27], v[236:237] op_sel_hi:[1,0,0]
	v_pk_fma_f32 v[128:129], v[72:73], s[26:27], v[236:237] op_sel_hi:[1,0,0]
	v_mfma_f32_32x32x16_bf16 v[48:63], v[132:135], v[238:241], v[48:63]
	v_exp_f32_e32 v214, v89
	v_exp_f32_e32 v213, v91
	v_exp_f32_e32 v207, v94
	v_pk_fma_f32 v[132:133], v[68:69], s[26:27], v[236:237] op_sel_hi:[1,0,0]
	v_pk_fma_f32 v[134:135], v[78:79], s[26:27], v[236:237] op_sel_hi:[1,0,0]
	v_mfma_f32_32x32x16_bf16 v[48:63], v[136:139], v[242:245], v[48:63]
	v_pk_fma_f32 v[138:139], v[64:65], s[26:27], v[236:237] op_sel_hi:[1,0,0]
	v_pk_fma_f32 v[136:137], v[66:67], s[26:27], v[236:237] op_sel_hi:[1,0,0]
	v_pk_fma_f32 v[162:163], v[74:75], s[26:27], v[236:237] op_sel_hi:[1,0,0]
	v_pk_fma_f32 v[160:161], v[76:77], s[26:27], v[236:237] op_sel_hi:[1,0,0]
	v_mfma_f32_32x32x16_bf16 v[48:63], v[208:211], v[246:249], v[48:63]
	v_exp_f32_e32 v211, v90
	v_exp_f32_e32 v208, v92
	v_exp_f32_e32 v210, v93
	v_exp_f32_e32 v209, v95
	v_add_f32_e32 v64, v203, v204
	v_fmac_f32_e32 v64, v197, v140
	v_add_f32_e32 v140, v215, v216
	s_addk_i32 s13, 0x80
	s_addk_i32 s14, 0x80
	v_fmac_f32_e32 v140, v64, v206
	s_cbranch_vccz .LBB0_2020
	s_and_saveexec_b64 s[10:11], s[4:5]
	ds_write_b32 v189, v205 offset:128
	s_or_b64 exec, exec, s[10:11]
	s_waitcnt lgkmcnt(0)
	v_add_u32_e32 v164, s12, v169
	ds_read_b128 v[238:241], v164 offset:224
	ds_read_b128 v[242:245], v164 offset:192
	ds_read_b128 v[246:249], v164 offset:160
	ds_read_b128 v[250:253], v164 offset:128
	s_waitcnt lgkmcnt(3)
	v_pk_mul_f32 v[12:13], v[12:13], v[238:239]
	s_waitcnt lgkmcnt(2)
	v_pk_mul_f32 v[8:9], v[8:9], v[242:243]
	s_waitcnt lgkmcnt(1)
	v_pk_mul_f32 v[4:5], v[4:5], v[246:247]
	v_pk_mul_f32 v[14:15], v[14:15], v[240:241]
	v_pk_mul_f32 v[10:11], v[10:11], v[244:245]
	v_pk_mul_f32 v[6:7], v[6:7], v[248:249]
	s_waitcnt lgkmcnt(0)
	v_pk_mul_f32 v[2:3], v[2:3], v[252:253]
	v_pk_mul_f32 v[0:1], v[0:1], v[250:251]
	v_pk_mul_f32 v[44:45], v[44:45], v[238:239]
	v_pk_mul_f32 v[40:41], v[40:41], v[242:243]
	v_pk_mul_f32 v[36:37], v[36:37], v[246:247]
	v_pk_mul_f32 v[46:47], v[46:47], v[240:241]
	v_pk_mul_f32 v[42:43], v[42:43], v[244:245]
	v_pk_mul_f32 v[38:39], v[38:39], v[248:249]
	v_pk_mul_f32 v[34:35], v[34:35], v[252:253]
	v_pk_mul_f32 v[32:33], v[32:33], v[250:251]
	v_pk_mul_f32 v[28:29], v[28:29], v[238:239]
	v_pk_mul_f32 v[24:25], v[24:25], v[242:243]
	v_pk_mul_f32 v[20:21], v[20:21], v[246:247]
	v_pk_mul_f32 v[30:31], v[30:31], v[240:241]
	v_pk_mul_f32 v[26:27], v[26:27], v[244:245]
	v_pk_mul_f32 v[22:23], v[22:23], v[248:249]
	v_pk_mul_f32 v[18:19], v[18:19], v[252:253]
	v_pk_mul_f32 v[16:17], v[16:17], v[250:251]
	v_pk_mul_f32 v[60:61], v[60:61], v[238:239]
	v_pk_mul_f32 v[56:57], v[56:57], v[242:243]
	v_pk_mul_f32 v[52:53], v[52:53], v[246:247]
	v_pk_mul_f32 v[62:63], v[62:63], v[240:241]
	v_pk_mul_f32 v[58:59], v[58:59], v[244:245]
	v_pk_mul_f32 v[54:55], v[54:55], v[248:249]
	v_pk_mul_f32 v[50:51], v[50:51], v[252:253]
	v_pk_mul_f32 v[48:49], v[48:49], v[250:251]
